# speedup vs baseline: 1.1708x; 1.0449x over previous
_Z9fc_kernelPKDv8_DF16_S1_Pf:
	s_cmp_gt_u32 s2, 195
	s_cbranch_scc1 .Lfc_exit
	s_load_dwordx4 s[4:7], s[0:1], 0x0
	s_load_dwordx2 s[16:17], s[0:1], 0x10
	v_and_b32_e32 v1, 63, v0
	v_lshrrev_b32_e32 v113, 6, v0
	v_and_b32_e32 v89, 31, v0
	v_bfe_u32 v90, v0, 5, 1
	v_lshlrev_b32_e32 v116, 4, v0
	v_lshlrev_b32_e32 v112, 4, v1
	v_lshlrev_b32_e32 v4, 12, v90
	v_lshl_or_b32 v4, v113, 8, v4
	v_lshl_or_b32 v4, v89, 2, v4
	v_add_u32_e32 v102, 0x1c000, v4
	v_lshlrev_b32_e32 v5, 13, v113
	s_mov_b32 s3, 0x1c000
	v_add3_u32 v103, v5, v112, s3
	v_mul_u32_u24_e32 v6, 0x186a00, v113
	v_add_u32_e32 v104, v6, v112
	v_add_u32_e32 v105, 0x30d40, v104
	v_add_u32_e32 v106, 0x61a80, v104
	v_add_u32_e32 v107, 0x927c0, v104
	v_add_u32_e32 v108, 0xc3500, v104
	v_add_u32_e32 v109, 0xf4240, v104
	v_add_u32_e32 v110, 0x124f80, v104
	v_add_u32_e32 v111, 0x155cc0, v104
	v_mul_u32_u24_e32 v7, 0x3800, v113
	v_add_u32_e32 v114, v7, v112
	v_cmp_gt_u32_e64 s[34:35], 20, v1
	s_mul_i32 s3, s2, 0xe000
	v_add_u32_e32 v117, s3, v114
	v_add_u32_e32 v118, 0x1000, v117
	v_add_u32_e32 v119, 0x2000, v117
	v_add_u32_e32 v115, 0x3000, v117
	s_waitcnt lgkmcnt(0)
	global_load_dwordx4 v[32:35], v117, s[4:5]
	global_load_dwordx4 v[36:39], v117, s[4:5] offset:1024
	global_load_dwordx4 v[40:43], v117, s[4:5] offset:2048
	global_load_dwordx4 v[44:47], v117, s[4:5] offset:3072
	global_load_dwordx4 v[48:51], v118, s[4:5]
	global_load_dwordx4 v[52:55], v118, s[4:5] offset:1024
	global_load_dwordx4 v[56:59], v118, s[4:5] offset:2048
	global_load_dwordx4 v[60:63], v118, s[4:5] offset:3072
	global_load_dwordx4 v[64:67], v119, s[4:5]
	global_load_dwordx4 v[68:71], v119, s[4:5] offset:1024
	global_load_dwordx4 v[72:75], v119, s[4:5] offset:2048
	global_load_dwordx4 v[76:79], v119, s[4:5] offset:3072
	global_load_dwordx4 v[80:83], v115, s[4:5]
	global_load_dwordx4 v[84:87], v115, s[4:5] offset:1024
	s_mov_b64 s[30:31], s[6:7]
	global_load_dwordx4 v[152:155], v116, s[30:31]
	s_add_u32 s30, s30, 0x1000
	s_addc_u32 s31, s31, 0
	global_load_dwordx4 v[156:159], v116, s[30:31]
	s_add_u32 s30, s30, 0x1000
	s_addc_u32 s31, s31, 0
	global_load_dwordx4 v[160:163], v116, s[30:31]
	s_add_u32 s30, s30, 0x1000
	s_addc_u32 s31, s31, 0
	global_load_dwordx4 v[164:167], v116, s[30:31]
	s_add_u32 s30, s30, 0x1000
	s_addc_u32 s31, s31, 0
	global_load_dwordx4 v[168:171], v116, s[30:31]
	s_add_u32 s30, s30, 0x1000
	s_addc_u32 s31, s31, 0
	global_load_dwordx4 v[172:175], v116, s[30:31]
	s_add_u32 s30, s30, 0x1000
	s_addc_u32 s31, s31, 0
	global_load_dwordx4 v[176:179], v116, s[30:31]
	s_add_u32 s30, s30, 0x1000
	s_addc_u32 s31, s31, 0
	global_load_dwordx4 v[180:183], v116, s[30:31]
	s_add_u32 s30, s30, 0x1000
	s_addc_u32 s31, s31, 0
	global_load_dwordx4 v[184:187], v116, s[30:31]
	s_add_u32 s30, s30, 0x1000
	s_addc_u32 s31, s31, 0
	global_load_dwordx4 v[188:191], v116, s[30:31]
	s_add_u32 s30, s30, 0x1000
	s_addc_u32 s31, s31, 0
	global_load_dwordx4 v[192:195], v116, s[30:31]
	s_add_u32 s30, s30, 0x1000
	s_addc_u32 s31, s31, 0
	global_load_dwordx4 v[196:199], v116, s[30:31]
	s_add_u32 s30, s30, 0x1000
	s_addc_u32 s31, s31, 0
	global_load_dwordx4 v[200:203], v116, s[30:31]
	s_add_u32 s30, s30, 0x1000
	s_addc_u32 s31, s31, 0
	global_load_dwordx4 v[204:207], v116, s[30:31]
	s_lshl_b32 s3, s2, 10
	s_add_u32 s8, s16, s3
	s_addc_u32 s9, s17, 0
	s_mov_b64 s[24:25], -1
	s_cmp_eq_u32 s2, 195
	s_cselect_b64 s[24:25], s[34:35], s[24:25]
	s_mov_b32 s20, 0
	s_waitcnt vmcnt(0)
	ds_write_b128 v116, v[152:155]
	ds_write_b128 v116, v[156:159] offset:4096
	ds_write_b128 v116, v[160:163] offset:8192
	ds_write_b128 v116, v[164:167] offset:12288
	ds_write_b128 v116, v[168:171] offset:16384
	ds_write_b128 v116, v[172:175] offset:20480
	ds_write_b128 v116, v[176:179] offset:24576
	ds_write_b128 v116, v[180:183] offset:28672
	ds_write_b128 v116, v[184:187] offset:32768
	ds_write_b128 v116, v[188:191] offset:36864
	ds_write_b128 v116, v[192:195] offset:40960
	ds_write_b128 v116, v[196:199] offset:45056
	ds_write_b128 v116, v[200:203] offset:49152
	ds_write_b128 v116, v[204:207] offset:53248
	s_waitcnt lgkmcnt(0)
	s_barrier

.Lfc_nopf:
	s_and_b32 s3, s20, 1
	s_mul_i32 s3, s3, 0xe000
	v_add_u32_e32 v88, s3, v112
	ds_read_b128 v[120:123], v88
	ds_read_b128 v[124:127], v88 offset:1024
	ds_read_b128 v[128:131], v88 offset:2048
	ds_read_b128 v[132:135], v88 offset:3072
	ds_read_b128 v[136:139], v88 offset:4096
	ds_read_b128 v[140:143], v88 offset:5120
	ds_read_b128 v[144:147], v88 offset:6144
	v_add_u32_e32 v88, 0x1c00, v88
	s_mov_b32 s0, 0
	s_waitcnt lgkmcnt(0)
.Lfc_step:
	v_mfma_f32_32x32x16_f16 v[0:15], v[120:123], v[32:35], 0
	v_mfma_f32_32x32x16_f16 v[16:31], v[120:123], v[60:63], 0
	v_mfma_f32_32x32x16_f16 v[0:15], v[124:127], v[36:39], v[0:15]
	v_mfma_f32_32x32x16_f16 v[16:31], v[124:127], v[64:67], v[16:31]
	v_mfma_f32_32x32x16_f16 v[0:15], v[128:131], v[40:43], v[0:15]
	v_mfma_f32_32x32x16_f16 v[16:31], v[128:131], v[68:71], v[16:31]
	v_mfma_f32_32x32x16_f16 v[0:15], v[132:135], v[44:47], v[0:15]
	v_mfma_f32_32x32x16_f16 v[16:31], v[132:135], v[72:75], v[16:31]
	v_mfma_f32_32x32x16_f16 v[0:15], v[136:139], v[48:51], v[0:15]
	v_mfma_f32_32x32x16_f16 v[16:31], v[136:139], v[76:79], v[16:31]
	v_mfma_f32_32x32x16_f16 v[0:15], v[140:143], v[52:55], v[0:15]
	v_mfma_f32_32x32x16_f16 v[16:31], v[140:143], v[80:83], v[16:31]
	v_mfma_f32_32x32x16_f16 v[0:15], v[144:147], v[56:59], v[0:15]
	v_mfma_f32_32x32x16_f16 v[16:31], v[144:147], v[84:87], v[16:31]
	s_nop 11
	s_barrier
	ds_write_b32 v102, v0 offset:0
	ds_write_b32 v102, v1 offset:1024
	ds_write_b32 v102, v2 offset:2048
	ds_write_b32 v102, v3 offset:3072
	ds_write_b32 v102, v4 offset:8192
	ds_write_b32 v102, v5 offset:9216
	ds_write_b32 v102, v6 offset:10240
	ds_write_b32 v102, v7 offset:11264
	ds_write_b32 v102, v8 offset:16384
	ds_write_b32 v102, v9 offset:17408
	ds_write_b32 v102, v10 offset:18432
	ds_write_b32 v102, v11 offset:19456
	ds_write_b32 v102, v12 offset:24576
	ds_write_b32 v102, v13 offset:25600
	ds_write_b32 v102, v14 offset:26624
	ds_write_b32 v102, v15 offset:27648
	ds_write_b32 v102, v16 offset:128
	ds_write_b32 v102, v17 offset:1152
	ds_write_b32 v102, v18 offset:2176
	ds_write_b32 v102, v19 offset:3200
	ds_write_b32 v102, v20 offset:8320
	ds_write_b32 v102, v21 offset:9344
	ds_write_b32 v102, v22 offset:10368
	ds_write_b32 v102, v23 offset:11392
	ds_write_b32 v102, v24 offset:16512
	ds_write_b32 v102, v25 offset:17536
	ds_write_b32 v102, v26 offset:18560
	ds_write_b32 v102, v27 offset:19584
	ds_write_b32 v102, v28 offset:24704
	ds_write_b32 v102, v29 offset:25728
	ds_write_b32 v102, v30 offset:26752
	ds_write_b32 v102, v31 offset:27776
	s_waitcnt lgkmcnt(0)
	s_barrier
	ds_read_b128 v[120:123], v88
	ds_read_b128 v[124:127], v88 offset:1024
	ds_read_b128 v[128:131], v88 offset:2048
	ds_read_b128 v[132:135], v88 offset:3072
	ds_read_b128 v[136:139], v88 offset:4096
	ds_read_b128 v[140:143], v88 offset:5120
	ds_read_b128 v[144:147], v88 offset:6144
	v_add_u32_e32 v88, 0x1c00, v88
	ds_read_b128 v[0:3], v103
	ds_read_b128 v[4:7], v103 offset:1024
	ds_read_b128 v[8:11], v103 offset:2048
	ds_read_b128 v[12:15], v103 offset:3072
	ds_read_b128 v[16:19], v103 offset:4096
	ds_read_b128 v[20:23], v103 offset:5120
	ds_read_b128 v[24:27], v103 offset:6144
	ds_read_b128 v[28:31], v103 offset:7168
	s_mov_b64 exec, s[24:25]
	s_waitcnt lgkmcnt(7)
	global_store_dwordx4 v104, v[0:3], s[8:9] nt
	s_waitcnt lgkmcnt(6)
	global_store_dwordx4 v105, v[4:7], s[8:9] nt
	s_waitcnt lgkmcnt(5)
	global_store_dwordx4 v106, v[8:11], s[8:9] nt
	s_waitcnt lgkmcnt(4)
	global_store_dwordx4 v107, v[12:15], s[8:9] nt
	s_waitcnt lgkmcnt(3)
	global_store_dwordx4 v108, v[16:19], s[8:9] nt
	s_waitcnt lgkmcnt(2)
	global_store_dwordx4 v109, v[20:23], s[8:9] nt
	s_waitcnt lgkmcnt(1)
	global_store_dwordx4 v110, v[24:27], s[8:9] nt
	s_waitcnt lgkmcnt(0)
	global_store_dwordx4 v111, v[28:31], s[8:9] nt
	s_mov_b64 exec, -1
	s_waitcnt vmcnt(8)
	s_add_u32 s8, s8, 0x61a800
	s_addc_u32 s9, s9, 0
	s_add_i32 s0, s0, 1
	s_cmp_lt_u32 s0, 8
	s_cbranch_scc1 .Lfc_step
	s_cmp_eq_u32 s20, 15
	s_cbranch_scc1 .Lfc_exit
	s_waitcnt vmcnt(63)
	s_add_i32 s3, s20, 1
	s_and_b32 s3, s3, 1
	s_mul_i32 s3, s3, 0xe000
	v_add_u32_e32 v117, s3, v116
	ds_write_b128 v117, v[152:155]
	ds_write_b128 v117, v[156:159] offset:4096
	ds_write_b128 v117, v[160:163] offset:8192
	ds_write_b128 v117, v[164:167] offset:12288
	ds_write_b128 v117, v[168:171] offset:16384
	ds_write_b128 v117, v[172:175] offset:20480
	ds_write_b128 v117, v[176:179] offset:24576
	ds_write_b128 v117, v[180:183] offset:28672
	ds_write_b128 v117, v[184:187] offset:32768
	ds_write_b128 v117, v[188:191] offset:36864
	ds_write_b128 v117, v[192:195] offset:40960
	ds_write_b128 v117, v[196:199] offset:45056
	ds_write_b128 v117, v[200:203] offset:49152
	ds_write_b128 v117, v[204:207] offset:53248
	s_waitcnt lgkmcnt(0)
	s_barrier
	s_add_i32 s20, s20, 1
	s_branch .Lfc_seg

	.amdhsa_kernel _Z9fc_kernelPKDv8_DF16_S1_Pf
		.amdhsa_group_segment_fixed_size 147456
		.amdhsa_private_segment_fixed_size 0
		.amdhsa_kernarg_size 24
		.amdhsa_user_sgpr_count 2
		.amdhsa_user_sgpr_dispatch_ptr 0
		.amdhsa_user_sgpr_queue_ptr 0
		.amdhsa_user_sgpr_kernarg_segment_ptr 1
		.amdhsa_user_sgpr_dispatch_id 0
		.amdhsa_user_sgpr_kernarg_preload_length 0
		.amdhsa_user_sgpr_kernarg_preload_offset 0
		.amdhsa_user_sgpr_private_segment_size 0
		.amdhsa_uses_dynamic_stack 0
		.amdhsa_enable_private_segment 0
		.amdhsa_system_sgpr_workgroup_id_x 1
		.amdhsa_system_sgpr_workgroup_id_y 0
		.amdhsa_system_sgpr_workgroup_id_z 0
		.amdhsa_system_sgpr_workgroup_info 0
		.amdhsa_system_vgpr_workitem_id 0
		.amdhsa_next_free_vgpr 208
		.amdhsa_next_free_sgpr 96
		.amdhsa_accum_offset 208
		.amdhsa_reserve_vcc 1
		.amdhsa_float_round_mode_32 0
		.amdhsa_float_round_mode_16_64 0
		.amdhsa_float_denorm_mode_32 3
		.amdhsa_float_denorm_mode_16_64 3
		.amdhsa_dx10_clamp 1
		.amdhsa_ieee_mode 1
		.amdhsa_fp16_overflow 0
		.amdhsa_tg_split 0
		.amdhsa_exception_fp_ieee_invalid_op 0
		.amdhsa_exception_fp_denorm_src 0
		.amdhsa_exception_fp_ieee_div_zero 0
		.amdhsa_exception_fp_ieee_overflow 0
		.amdhsa_exception_fp_ieee_underflow 0
		.amdhsa_exception_fp_ieee_inexact 0
		.amdhsa_exception_int_div_zero 0
	.end_amdhsa_kernel

amdhsa.kernels:
  - .agpr_count:     0
    .args:
      - .actual_access:  read_only
        .address_space:  global
        .offset:         0
        .size:           8
        .value_kind:     global_buffer
      - .actual_access:  read_only
        .address_space:  global
        .offset:         8
        .size:           8
        .value_kind:     global_buffer
      - .actual_access:  read_only
        .address_space:  global
        .offset:         16
        .size:           8
        .value_kind:     global_buffer
      - .actual_access:  read_only
        .address_space:  global
        .offset:         24
        .size:           8
        .value_kind:     global_buffer
      - .actual_access:  read_only
        .address_space:  global
        .offset:         32
        .size:           8
        .value_kind:     global_buffer
      - .actual_access:  write_only
        .address_space:  global
        .offset:         40
        .size:           8
        .value_kind:     global_buffer
      - .actual_access:  write_only
        .address_space:  global
        .offset:         48
        .size:           8
        .value_kind:     global_buffer
      - .actual_access:  write_only
        .address_space:  global
        .offset:         56
        .size:           8
        .value_kind:     global_buffer
    .group_segment_fixed_size: 0
    .kernarg_segment_align: 8
    .kernarg_segment_size: 64
    .language:       OpenCL C
    .language_version:
      - 2
      - 0
    .max_flat_workgroup_size: 256
    .name:           _Z11prep_kernelPKfS0_S0_S0_S0_PDv8_DF16_S2_Pi
    .private_segment_fixed_size: 0
    .sgpr_count:     26
    .sgpr_spill_count: 0
    .symbol:         _Z11prep_kernelPKfS0_S0_S0_S0_PDv8_DF16_S2_Pi.kd
    .uniform_work_group_size: 1
    .uses_dynamic_stack: false
    .vgpr_count:     18
    .vgpr_spill_count: 0
    .wavefront_size: 64
  - .agpr_count:     0
    .args:
      - .actual_access:  read_only
        .address_space:  global
        .offset:         0
        .size:           8
        .value_kind:     global_buffer
      - .actual_access:  read_only
        .address_space:  global
        .offset:         8
        .size:           8
        .value_kind:     global_buffer
      - .actual_access:  read_only
        .address_space:  global
        .offset:         16
        .size:           8
        .value_kind:     global_buffer
      - .actual_access:  read_only
        .address_space:  global
        .offset:         24
        .size:           8
        .value_kind:     global_buffer
      - .actual_access:  read_only
        .address_space:  global
        .offset:         32
        .size:           8
        .value_kind:     global_buffer
      - .actual_access:  read_only
        .address_space:  global
        .offset:         40
        .size:           8
        .value_kind:     global_buffer
      - .actual_access:  read_only
        .address_space:  global
        .offset:         48
        .size:           8
        .value_kind:     global_buffer
      - .actual_access:  read_only
        .address_space:  global
        .offset:         56
        .size:           8
        .value_kind:     global_buffer
      - .actual_access:  read_only
        .address_space:  global
        .offset:         64
        .size:           8
        .value_kind:     global_buffer
      - .actual_access:  read_only
        .address_space:  global
        .offset:         72
        .size:           8
        .value_kind:     global_buffer
      - .actual_access:  read_only
        .address_space:  global
        .offset:         80
        .size:           8
        .value_kind:     global_buffer
      - .actual_access:  read_only
        .address_space:  global
        .offset:         88
        .size:           8
        .value_kind:     global_buffer
      - .actual_access:  read_only
        .address_space:  global
        .offset:         96
        .size:           8
        .value_kind:     global_buffer
      - .actual_access:  read_only
        .address_space:  global
        .offset:         104
        .size:           8
        .value_kind:     global_buffer
      - .actual_access:  write_only
        .address_space:  global
        .offset:         112
        .size:           8
        .value_kind:     global_buffer
      - .offset:         120
        .size:           4
        .value_kind:     by_value
      - .actual_access:  read_only
        .address_space:  global
        .offset:         128
        .size:           8
        .value_kind:     global_buffer
      - .actual_access:  read_only
        .address_space:  global
        .offset:         136
        .size:           8
        .value_kind:     global_buffer
      - .actual_access:  write_only
        .address_space:  global
        .offset:         144
        .size:           8
        .value_kind:     global_buffer
      - .actual_access:  read_only
        .address_space:  global
        .offset:         152
        .size:           8
        .value_kind:     global_buffer
      - .actual_access:  read_only
        .address_space:  global
        .offset:         160
        .size:           8
        .value_kind:     global_buffer
      - .address_space:  global
        .offset:         168
        .size:           8
        .value_kind:     global_buffer
      - .actual_access:  write_only
        .address_space:  global
        .offset:         176
        .size:           8
        .value_kind:     global_buffer
      - .address_space:  global
        .offset:         184
        .size:           8
        .value_kind:     global_buffer
      - .actual_access:  write_only
        .address_space:  global
        .offset:         192
        .size:           8
        .value_kind:     global_buffer
      - .actual_access:  write_only
        .address_space:  global
        .offset:         200
        .size:           8
        .value_kind:     global_buffer
    .group_segment_fixed_size: 21760
    .kernarg_segment_align: 8
    .kernarg_segment_size: 208
    .language:       OpenCL C
    .language_version:
      - 2
      - 0
    .max_flat_workgroup_size: 256
    .name:           _Z12embed_kernelPKiS0_S0_S0_S0_PKfS2_S2_S2_S2_S2_S2_S2_PKDv8_DF16_PfiS2_S2_PS3_S0_S0_PiS8_S8_P15HIP_vector_typeIiLj2EES8_
    .private_segment_fixed_size: 0
    .sgpr_count:     44
    .sgpr_spill_count: 0
    .symbol:         _Z12embed_kernelPKiS0_S0_S0_S0_PKfS2_S2_S2_S2_S2_S2_S2_PKDv8_DF16_PfiS2_S2_PS3_S0_S0_PiS8_S8_P15HIP_vector_typeIiLj2EES8_.kd
    .uniform_work_group_size: 1
    .uses_dynamic_stack: false
    .vgpr_count:     166
    .vgpr_spill_count: 0
    .wavefront_size: 64
  - .agpr_count:     0
    .args:
      - .actual_access:  read_only
        .address_space:  global
        .offset:         0
        .size:           8
        .value_kind:     global_buffer
      - .actual_access:  read_only
        .address_space:  global
        .offset:         8
        .size:           8
        .value_kind:     global_buffer
      - .actual_access:  read_only
        .address_space:  global
        .offset:         16
        .size:           8
        .value_kind:     global_buffer
      - .actual_access:  read_only
        .address_space:  global
        .offset:         24
        .size:           8
        .value_kind:     global_buffer
      - .actual_access:  read_only
        .address_space:  global
        .offset:         32
        .size:           8
        .value_kind:     global_buffer
      - .actual_access:  read_only
        .address_space:  global
        .offset:         40
        .size:           8
        .value_kind:     global_buffer
      - .actual_access:  read_only
        .address_space:  global
        .offset:         48
        .size:           8
        .value_kind:     global_buffer
      - .actual_access:  read_only
        .address_space:  global
        .offset:         56
        .size:           8
        .value_kind:     global_buffer
      - .actual_access:  write_only
        .address_space:  global
        .offset:         64
        .size:           8
        .value_kind:     global_buffer
      - .offset:         72
        .size:           4
        .value_kind:     by_value
    .group_segment_fixed_size: 30720
    .kernarg_segment_align: 8
    .kernarg_segment_size: 76
    .language:       OpenCL C
    .language_version:
      - 2
      - 0
    .max_flat_workgroup_size: 256
    .name:           _Z10gru_kernelPKfPKiS2_S2_PK15HIP_vector_typeIiLj2EEPKDv8_DF16_S0_S0_Pfi
    .private_segment_fixed_size: 0
    .sgpr_count:     31
    .sgpr_spill_count: 0
    .symbol:         _Z10gru_kernelPKfPKiS2_S2_PK15HIP_vector_typeIiLj2EEPKDv8_DF16_S0_S0_Pfi.kd
    .uniform_work_group_size: 1
    .uses_dynamic_stack: false
    .vgpr_count:     231
    .vgpr_spill_count: 0
    .wavefront_size: 64
  - .agpr_count:     0
    .args:
      - .actual_access:  read_only
        .address_space:  global
        .offset:         0
        .size:           8
        .value_kind:     global_buffer
      - .actual_access:  read_only
        .address_space:  global
        .offset:         8
        .size:           8
        .value_kind:     global_buffer
      - .actual_access:  write_only
        .address_space:  global
        .offset:         16
        .size:           8
        .value_kind:     global_buffer
    .group_segment_fixed_size: 1024
    .kernarg_segment_align: 8
    .kernarg_segment_size: 24
    .language:       OpenCL C
    .language_version:
      - 2
      - 0
    .max_flat_workgroup_size: 256
    .name:           _Z11pool_kernelPKfPKiPDF16_
    .private_segment_fixed_size: 0
    .sgpr_count:     26
    .sgpr_spill_count: 0
    .symbol:         _Z11pool_kernelPKfPKiPDF16_.kd
    .uniform_work_group_size: 1
    .uses_dynamic_stack: false
    .vgpr_count:     31
    .vgpr_spill_count: 0
    .wavefront_size: 64
  - .agpr_count:     0
    .args:
      - .actual_access:  read_only
        .address_space:  global
        .offset:         0
        .size:           8
        .value_kind:     global_buffer
      - .actual_access:  read_only
        .address_space:  global
        .offset:         8
        .size:           8
        .value_kind:     global_buffer
      - .actual_access:  write_only
        .address_space:  global
        .offset:         16
        .size:           8
        .value_kind:     global_buffer
    .group_segment_fixed_size: 147456
    .kernarg_segment_align: 8
    .kernarg_segment_size: 24
    .language:       OpenCL C
    .language_version:
      - 2
      - 0
    .max_flat_workgroup_size: 256
    .name:           _Z9fc_kernelPKDv8_DF16_S1_Pf
    .private_segment_fixed_size: 0
    .sgpr_count:     17
    .sgpr_spill_count: 0
    .symbol:         _Z9fc_kernelPKDv8_DF16_S1_Pf.kd
    .uniform_work_group_size: 1
    .uses_dynamic_stack: false
    .vgpr_count:     208
    .vgpr_spill_count: 0
    .wavefront_size: 64
